# speedup vs baseline: 1.0065x; 1.0065x over previous
.Lh_no_cnt:
	v_mov_b32_e32 v43, v38
	s_waitcnt vmcnt(2)
	v_cmp_lt_f32_e64 s[34:35], |v2|, s48
	v_cmp_lt_f32_e64 s[36:37], |v3|, s48
	v_cmp_lt_f32_e64 s[38:39], |v4|, s48
	v_cmp_lt_f32_e64 s[40:41], |v5|, s48
	s_and_b64 s[34:35], s[34:35], s[26:27]
	s_and_b64 s[36:37], s[36:37], s[28:29]
	s_and_b64 s[38:39], s[38:39], s[30:31]
	s_and_b64 s[40:41], s[40:41], s[32:33]
	v_mbcnt_lo_u32_b32 v28, s34, 0
	v_mbcnt_lo_u32_b32 v29, s36, 0
	v_mbcnt_lo_u32_b32 v30, s38, 0
	v_mbcnt_lo_u32_b32 v31, s40, 0
	v_mbcnt_hi_u32_b32 v28, s35, v28
	v_mbcnt_hi_u32_b32 v29, s37, v29
	v_mbcnt_hi_u32_b32 v30, s39, v30
	v_mbcnt_hi_u32_b32 v31, s41, v31
	s_bcnt1_i32_b64 s54, s[34:35]
	s_bcnt1_i32_b64 s55, s[36:37]
	s_bcnt1_i32_b64 s56, s[38:39]
	s_bcnt1_i32_b64 s57, s[40:41]
	s_lshl2_add_u32 s58, s42, s46
	v_lshl_add_u32 v28, v28, 2, s58
	s_lshl2_add_u32 s58, s54, s58
	v_lshl_add_u32 v29, v29, 2, s58
	s_lshl2_add_u32 s58, s55, s58
	v_lshl_add_u32 v30, v30, 2, s58
	s_lshl2_add_u32 s58, s56, s58
	v_lshl_add_u32 v31, v31, 2, s58
	s_add_i32 s54, s54, s55
	s_add_i32 s56, s56, s57
	s_add_i32 s42, s42, s54
	s_add_i32 s42, s42, s56
	s_mov_b64 exec, s[34:35]
	ds_write_b32 v28, v2
	s_mov_b64 exec, s[36:37]
	ds_write_b32 v29, v3
	s_mov_b64 exec, s[38:39]
	ds_write_b32 v30, v4
	s_mov_b64 exec, s[40:41]
	ds_write_b32 v31, v5
	s_mov_b64 exec, -1
	s_branch .Lh_loop_entry
.Lh_stage1:
	s_setprio 2
	s_mov_b32 s47, 1
	s_mov_b32 s42, 0
	s_mov_b32 s43, 0
	v_lshl_add_u32 v26, v1, 2, s46
	v_mov_b32_e32 v43, v39
	s_waitcnt vmcnt(1)
	v_cmp_lt_f32_e64 s[34:35], |v6|, s48
	v_cmp_lt_f32_e64 s[36:37], |v7|, s48
	v_cmp_lt_f32_e64 s[38:39], |v8|, s48
	v_cmp_lt_f32_e64 s[40:41], |v9|, s48
	s_and_b64 s[34:35], s[34:35], s[26:27]
	s_and_b64 s[36:37], s[36:37], s[28:29]
	s_and_b64 s[38:39], s[38:39], s[30:31]
	s_and_b64 s[40:41], s[40:41], s[32:33]
	v_mbcnt_lo_u32_b32 v28, s34, 0
	v_mbcnt_lo_u32_b32 v29, s36, 0
	v_mbcnt_lo_u32_b32 v30, s38, 0
	v_mbcnt_lo_u32_b32 v31, s40, 0
	v_mbcnt_hi_u32_b32 v28, s35, v28
	v_mbcnt_hi_u32_b32 v29, s37, v29
	v_mbcnt_hi_u32_b32 v30, s39, v30
	v_mbcnt_hi_u32_b32 v31, s41, v31
	s_bcnt1_i32_b64 s54, s[34:35]
	s_bcnt1_i32_b64 s55, s[36:37]
	s_bcnt1_i32_b64 s56, s[38:39]
	s_bcnt1_i32_b64 s57, s[40:41]
	s_lshl2_add_u32 s58, s42, s46
	v_lshl_add_u32 v28, v28, 2, s58
	s_lshl2_add_u32 s58, s54, s58
	v_lshl_add_u32 v29, v29, 2, s58
	s_lshl2_add_u32 s58, s55, s58
	v_lshl_add_u32 v30, v30, 2, s58
	s_lshl2_add_u32 s58, s56, s58
	v_lshl_add_u32 v31, v31, 2, s58
	s_add_i32 s54, s54, s55
	s_add_i32 s56, s56, s57
	s_add_i32 s42, s42, s54
	s_add_i32 s42, s42, s56
	s_mov_b64 exec, s[34:35]
	ds_write_b32 v28, v6
	s_mov_b64 exec, s[36:37]
	ds_write_b32 v29, v7
	s_mov_b64 exec, s[38:39]
	ds_write_b32 v30, v8
	s_mov_b64 exec, s[40:41]
	ds_write_b32 v31, v9
	s_mov_b64 exec, -1
	s_branch .Lh_loop_entry
.Lh_stage2:
	s_setprio 1
	s_mov_b32 s47, 2
	s_mov_b32 s42, 0
	s_mov_b32 s43, 0
	v_lshl_add_u32 v26, v1, 2, s46
	v_mov_b32_e32 v43, v40
	s_waitcnt vmcnt(0)
	v_cmp_lt_f32_e64 s[34:35], |v10|, s48
	v_cmp_lt_f32_e64 s[36:37], |v11|, s48
	v_cmp_lt_f32_e64 s[38:39], |v12|, s48
	v_cmp_lt_f32_e64 s[40:41], |v13|, s48
	s_and_b64 s[34:35], s[34:35], s[26:27]
	s_and_b64 s[36:37], s[36:37], s[28:29]
	s_and_b64 s[38:39], s[38:39], s[30:31]
	s_and_b64 s[40:41], s[40:41], s[32:33]
	v_mbcnt_lo_u32_b32 v28, s34, 0
	v_mbcnt_lo_u32_b32 v29, s36, 0
	v_mbcnt_lo_u32_b32 v30, s38, 0
	v_mbcnt_lo_u32_b32 v31, s40, 0
	v_mbcnt_hi_u32_b32 v28, s35, v28
	v_mbcnt_hi_u32_b32 v29, s37, v29
	v_mbcnt_hi_u32_b32 v30, s39, v30
	v_mbcnt_hi_u32_b32 v31, s41, v31
	s_bcnt1_i32_b64 s54, s[34:35]
	s_bcnt1_i32_b64 s55, s[36:37]
	s_bcnt1_i32_b64 s56, s[38:39]
	s_bcnt1_i32_b64 s57, s[40:41]
	s_lshl2_add_u32 s58, s42, s46
	v_lshl_add_u32 v28, v28, 2, s58
	s_lshl2_add_u32 s58, s54, s58
	v_lshl_add_u32 v29, v29, 2, s58
	s_lshl2_add_u32 s58, s55, s58
	v_lshl_add_u32 v30, v30, 2, s58
	s_lshl2_add_u32 s58, s56, s58
	v_lshl_add_u32 v31, v31, 2, s58
	s_add_i32 s54, s54, s55
	s_add_i32 s56, s56, s57
	s_add_i32 s42, s42, s54
	s_add_i32 s42, s42, s56
	s_mov_b64 exec, s[34:35]
	ds_write_b32 v28, v10
	s_mov_b64 exec, s[36:37]
	ds_write_b32 v29, v11
	s_mov_b64 exec, s[38:39]
	ds_write_b32 v30, v12
	s_mov_b64 exec, s[40:41]
	ds_write_b32 v31, v13
	s_mov_b64 exec, -1
	s_branch .Lh_loop_entry
.Lh_loop_entry:
	s_sub_i32 s59, s42, s43
	s_cmp_lt_i32 s59, 1
	s_cbranch_scc1 .Lh_loop_exit
	s_cmp_ge_i32 s59, 64
	s_cbranch_scc1 .Lh_loop_first
	s_bfm_b64 exec, s59, 0

.Lh_loop_body:
	v_fmamk_f32 v27, v24, 0x42000000, v41
	v_add_u32_e32 v26, 0x100, v26
	ds_read_b32 v24, v26
	s_add_i32 s43, s43, 64
	v_rndne_f32_e32 v28, v27
	v_sub_f32_e32 v29, v27, v28
	v_cvt_i32_f32_e32 v30, v28
	v_mul_f32_e32 v37, 0xbf38aa3b, v29
	v_fmamk_f32 v32, v29, 0x3fb8aa3b, v42
	v_fma_f32 v33, -v29, s51, v42
	v_fmaak_f32 v31, v29, v37, 0x41a00000
	v_lshl_add_u32 v30, v30, 6, v43
	v_exp_f32_e32 v31, v31
	v_exp_f32_e32 v32, v32
	v_exp_f32_e32 v33, v33
	v_cvt_rpi_i32_f32_e32 v36, v31
	ds_add_u32 v30, v36 offset:320
	v_mul_f32_e32 v34, v32, v31
	v_mul_f32_e32 v35, v33, v31
	v_cvt_rpi_i32_f32_e32 v36, v34
	v_cvt_rpi_i32_f32_e32 v37, v35
	ds_add_u32 v30, v36 offset:384
	ds_add_u32 v30, v37 offset:256
	v_mul_f32_e32 v32, 0x3ebc5ab2, v32
	v_mul_f32_e32 v33, 0x3ebc5ab2, v33
	v_mul_f32_e32 v34, v32, v34
	v_mul_f32_e32 v35, v33, v35
	v_cvt_rpi_i32_f32_e32 v36, v34
	v_cvt_rpi_i32_f32_e32 v37, v35
	ds_add_u32 v30, v36 offset:448
	ds_add_u32 v30, v37 offset:192
	v_mul_f32_e32 v32, 0x3ebc5ab2, v32
	v_mul_f32_e32 v33, 0x3ebc5ab2, v33
	v_mul_f32_e32 v34, v32, v34
	v_mul_f32_e32 v35, v33, v35
	v_cvt_rpi_i32_f32_e32 v36, v34
	v_cvt_rpi_i32_f32_e32 v37, v35
	ds_add_u32 v30, v36 offset:512
	ds_add_u32 v30, v37 offset:128
	v_mul_f32_e32 v32, 0x3ebc5ab2, v32
	v_mul_f32_e32 v33, 0x3ebc5ab2, v33
	v_mul_f32_e32 v34, v32, v34
	v_mul_f32_e32 v35, v33, v35
	v_cvt_rpi_i32_f32_e32 v36, v34
	v_cvt_rpi_i32_f32_e32 v37, v35
	ds_add_u32 v30, v36 offset:576
	ds_add_u32 v30, v37 offset:64
	v_mul_f32_e32 v32, 0x3ebc5ab2, v32
	v_mul_f32_e32 v33, 0x3ebc5ab2, v33
	v_mul_f32_e32 v34, v32, v34
	v_mul_f32_e32 v35, v33, v35
	v_cvt_rpi_i32_f32_e32 v36, v34
	v_cvt_rpi_i32_f32_e32 v37, v35
	ds_add_u32 v30, v36 offset:640
	ds_add_u32 v30, v37
	s_sub_i32 s59, s42, s43
	s_cmp_ge_i32 s59, 64
	s_waitcnt lgkmcnt(11)
	s_cbranch_scc1 .Lh_loop_body
	s_cmp_lt_i32 s59, 1
	s_cbranch_scc1 .Lh_loop_exit
	s_bfm_b64 exec, s59, 0
	s_branch .Lh_loop_body
.Lh_loop_exit:
	s_mov_b64 exec, -1
	s_cmp_eq_u32 s47, 0
	s_cbranch_scc1 .Lh_stage1
	s_cmp_eq_u32 s47, 1
	s_cbranch_scc1 .Lh_stage2
